# s_setprio 3 for the scan's MFMA waves during the scan loop
# baseline (speedup 1.0000x reference)
; DI void gdn_scan_seq(const Params& p, int bh16, char* ldsf) {
;     ...
;   f32x16 S[4];
; #pragma unroll
;   for (int m = 0; m < 4; ++m)
; #pragma unroll
;     for (int r = 0; r < 16; ++r) S[m][r] = 0.f;
;   asm volatile("s_waitcnt vmcnt(0)" ::: "memory");
;   __syncthreads();
;   SCAN_ISSUE(0, 0); SCAN_ISSUE(1, 1);
;   int sl = 0;
; #pragma unroll 1
;   for (int c = 0; c < 128; ++c) {
;     if (c + 1 < 128) asm volatile("s_waitcnt vmcnt(12)" ::: "memory"); else asm volatile("s_waitcnt vmcnt(0)" ::: "memory");
;     __builtin_amdgcn_s_barrier();
.Lscan_glt_done:
	s_or_b64 exec, exec, s[6:7]
	s_cmp_ge_u32 s16, 0x80
	s_cbranch_scc1 .Lscan_idle
	s_lshl_b32 s3, s2, 22
	s_add_u32 s8, s56, s3
	s_addc_u32 s9, s57, 0
	s_add_u32 s10, s8, 0x1000
	s_addc_u32 s11, s9, 0
	v_mov_b32_e32 v0, 0
	v_mov_b32_e32 v1, 0
	v_mov_b32_e32 v2, 0
	v_mov_b32_e32 v3, 0
	v_mov_b32_e32 v4, 0
	v_mov_b32_e32 v5, 0
	v_mov_b32_e32 v6, 0
	v_mov_b32_e32 v7, 0
	v_mov_b32_e32 v8, 0
	v_mov_b32_e32 v9, 0
	v_mov_b32_e32 v10, 0
	v_mov_b32_e32 v11, 0
	v_mov_b32_e32 v12, 0
	v_mov_b32_e32 v13, 0
	v_mov_b32_e32 v14, 0
	v_mov_b32_e32 v15, 0
	v_mov_b32_e32 v16, 0
	v_mov_b32_e32 v17, 0
	v_mov_b32_e32 v18, 0
	v_mov_b32_e32 v19, 0
	v_mov_b32_e32 v20, 0
	v_mov_b32_e32 v21, 0
	v_mov_b32_e32 v22, 0
	v_mov_b32_e32 v23, 0
	v_mov_b32_e32 v24, 0
	v_mov_b32_e32 v25, 0
	v_mov_b32_e32 v26, 0
	v_mov_b32_e32 v27, 0
	v_mov_b32_e32 v28, 0
	v_mov_b32_e32 v29, 0
	v_mov_b32_e32 v30, 0
	v_mov_b32_e32 v31, 0
	v_mov_b32_e32 v32, 0
	v_mov_b32_e32 v33, 0
	v_mov_b32_e32 v34, 0
	v_mov_b32_e32 v35, 0
	v_mov_b32_e32 v36, 0
	v_mov_b32_e32 v37, 0
	v_mov_b32_e32 v38, 0
	v_mov_b32_e32 v39, 0
	v_mov_b32_e32 v40, 0
	v_mov_b32_e32 v41, 0
	v_mov_b32_e32 v42, 0
	v_mov_b32_e32 v43, 0
	v_mov_b32_e32 v44, 0
	v_mov_b32_e32 v45, 0
	v_mov_b32_e32 v46, 0
	v_mov_b32_e32 v47, 0
	v_mov_b32_e32 v48, 0
	v_mov_b32_e32 v49, 0
	v_mov_b32_e32 v50, 0
	v_mov_b32_e32 v51, 0
	v_mov_b32_e32 v52, 0
	v_mov_b32_e32 v53, 0
	v_mov_b32_e32 v54, 0
	v_mov_b32_e32 v55, 0
	v_mov_b32_e32 v56, 0
	v_mov_b32_e32 v57, 0
	v_mov_b32_e32 v58, 0
	v_mov_b32_e32 v59, 0
	v_mov_b32_e32 v60, 0
	v_mov_b32_e32 v61, 0
	v_mov_b32_e32 v62, 0
	v_mov_b32_e32 v63, 0
	v_mov_b32_e32 v80, 0
	v_mov_b32_e32 v81, 0
	v_mov_b32_e32 v82, 0
	v_mov_b32_e32 v83, 0
	v_mov_b32_e32 v84, 0
	v_mov_b32_e32 v85, 0
	v_mov_b32_e32 v86, 0
	v_mov_b32_e32 v87, 0
	v_mov_b32_e32 v182, 0
	v_mov_b32_e32 v183, 0
	v_mov_b32_e32 v184, 0
	v_mov_b32_e32 v185, 0
	v_mov_b32_e32 v190, 0
	v_mov_b32_e32 v191, 0
	v_mov_b32_e32 v192, 0
	v_mov_b32_e32 v193, 0
	v_mov_b32_e32 v194, 0
	v_mov_b32_e32 v195, 0
	v_mov_b32_e32 v196, 0
	v_mov_b32_e32 v197, 0
	v_mov_b32_e32 v198, 0
	v_mov_b32_e32 v199, 0
	v_mov_b32_e32 v200, 0
	v_mov_b32_e32 v201, 0
	v_mov_b32_e32 v202, 0
	v_mov_b32_e32 v203, 0
	v_mov_b32_e32 v204, 0
	v_mov_b32_e32 v205, 0
	v_mov_b32_e32 v208, 0
	v_mov_b32_e32 v209, 0
	v_mov_b32_e32 v210, 0
	v_mov_b32_e32 v211, 0
	v_mov_b32_e32 v212, 0
	v_mov_b32_e32 v213, 0
	v_mov_b32_e32 v214, 0
	v_mov_b32_e32 v215, 0
	v_mov_b32_e32 v216, 0
	v_mov_b32_e32 v217, 0
	v_mov_b32_e32 v218, 0
	v_mov_b32_e32 v219, 0
	s_or_b32 s16, s16, s17
	s_lshl_b32 s3, s2, 6
	s_add_u32 s14, s84, s3
	s_addc_u32 s15, s85, 0
	s_add_u32 s14, s14, 0xc00
	s_addc_u32 s15, s15, 0
	v_mov_b32_e32 v132, 1
	v_mov_b32_e32 v133, 0
	s_mov_b32 s2, 0
	s_mov_b32 s3, 0
	s_mov_b32 s18, 0x24040
	s_waitcnt lgkmcnt(0)
	s_barrier
	s_setprio 3

; DI float bflo(unsigned u) { return __uint_as_float(u << 16); }
; DI float bfhi(unsigned u) { return __uint_as_float(u & 0xffff0000u); }
; DI bf16x8 packS(const f32x16& x, int s) { return pack8(x[8 * s], x[8 * s + 1], x[8 * s + 2], x[8 * s + 3], x[8 * s + 4], x[8 * s + 5], x[8 * s + 6], x[8 * s + 7]); }
; #define SCAN_RDW(F, mh) do { _Pragma("unroll") for (int k = 0; k < 8; ++k) { const int i2 = k >> 2, m = 2 * (mh) + ((k >> 1) & 1), sx = k & 1; F[k] = *(const bf16x8*)(lw + ((i2 * 4 + m) * 2 + sx) * 1024); } } while (0)
; DI void gdn_scan_seq(const Params& p, int bh16, char* ldsf) {
;     ...
;     char* sco = scp + (size_t)c * 32768;
;     bf16x8 Sb[4][2];
; #pragma unroll
;     for (int m = 0; m < 4; ++m) { Sb[m][0] = packS(S[m], 0); Sb[m][1] = packS(S[m], 1); *(bf16x8*)(sco + (m * 2 + 0) * 1024) = Sb[m][0]; *(bf16x8*)(sco + (m * 2 + 1) * 1024) = Sb[m][1]; }
;     __builtin_amdgcn_sched_barrier(0);
;     if (c + 2 < 128) { const int s2 = sl >= 1 ? sl - 1 : 2; SCAN_ISSUE(c + 2, s2); }
;     const char* base = ldsf + sl * 49152;
;     const char* lw = base + lane * 16; const char* lk = lw + 16384; const char* lu = base + 32768 + wv * 4096 + lane * 16;
;     const float gl = glt[c];
;     f32x16 vn[2];
; #pragma unroll
;     for (int i2 = 0; i2 < 2; ++i2) {
;       const u32x4 ua = *(const u32x4*)(lu + (2 * i2) * 1024), ub = *(const u32x4*)(lu + (2 * i2 + 1) * 1024);
; #pragma unroll
;       for (int e = 0; e < 4; ++e) { vn[i2][2 * e] = bflo(ua[e]); vn[i2][2 * e + 1] = bfhi(ua[e]); vn[i2][8 + 2 * e] = bflo(ub[e]); vn[i2][8 + 2 * e + 1] = bfhi(ub[e]); }
;     }
;     bf16x8 fa[8], fb[8];
;     ...
;     SCAN_RDW(fa, 0);
;     __builtin_amdgcn_sched_barrier(0);
;     SCAN_RDW(fb, 1);
;     __builtin_amdgcn_sched_barrier(0);
;     SCAN_MMW(fa, 0);
;     __builtin_amdgcn_sched_barrier(0);
;     SCAN_RDK(fa, 0);
;     __builtin_amdgcn_sched_barrier(0);
;     SCAN_MMW(fb, 1);
;     __builtin_amdgcn_sched_barrier(0);
;     SCAN_RDK(fb, 1);
;     __builtin_amdgcn_sched_barrier(0);
;     bf16x8 Vb[2][2];
; #pragma unroll
;     for (int j2 = 0; j2 < 2; ++j2) { Vb[j2][0] = packS(vn[j2], 0); Vb[j2][1] = packS(vn[j2], 1); }
; #pragma unroll
;     for (int m = 0; m < 4; ++m)
; #pragma unroll
;       for (int r = 0; r < 16; ++r) S[m][r] *= gl;
.Lscan_noprog:
	v_add_u32_e32 v131, s3, v130
	v_add_u32_e32 v134, s3, v129
	v_mov_b32_e32 v143, s18
	ds_read_b128 v[72:75], v134 offset:32768
	ds_read_b128 v[76:79], v134 offset:33792
	ds_read_b32 v142, v143
	ds_read_b128 v[148:151], v131 offset:0
	ds_read_b128 v[152:155], v131 offset:1024
	ds_read_b128 v[156:159], v131 offset:2048
	ds_read_b128 v[160:163], v131 offset:3072
	ds_read_b128 v[164:167], v131 offset:4096
	ds_read_b128 v[168:171], v131 offset:5120
	ds_read_b128 v[172:175], v131 offset:6144
	ds_read_b128 v[178:181], v131 offset:7168
	ds_read_b128 v[88:91], v134 offset:34816
	ds_read_b128 v[92:95], v134 offset:35840
	s_waitcnt lgkmcnt(10)
	v_mfma_f32_32x32x16_bf16 v[0:15], v[182:185], v[80:83], v[0:15]
	v_lshlrev_b32_e32 v64, 16, v72
	v_and_b32_e32 v65, 0xffff0000, v72
	v_lshlrev_b32_e32 v66, 16, v73
	v_and_b32_e32 v67, 0xffff0000, v73
	v_mfma_f32_32x32x16_bf16 v[0:15], v[190:193], v[84:87], v[0:15]
	v_lshlrev_b32_e32 v68, 16, v74
	v_and_b32_e32 v69, 0xffff0000, v74
	v_lshlrev_b32_e32 v70, 16, v75
	v_and_b32_e32 v71, 0xffff0000, v75
	v_mfma_f32_32x32x16_bf16 v[16:31], v[194:197], v[80:83], v[16:31]
	v_lshlrev_b32_e32 v72, 16, v76
	v_and_b32_e32 v73, 0xffff0000, v76
	v_lshlrev_b32_e32 v74, 16, v77
	v_and_b32_e32 v75, 0xffff0000, v77
	v_mfma_f32_32x32x16_bf16 v[16:31], v[198:201], v[84:87], v[16:31]
	v_lshlrev_b32_e32 v76, 16, v78
	v_and_b32_e32 v77, 0xffff0000, v78
	v_lshlrev_b32_e32 v78, 16, v79
	v_and_b32_e32 v79, 0xffff0000, v79
	s_waitcnt lgkmcnt(8)
	ds_read_b128 v[182:185], v131 offset:8192
	ds_read_b128 v[190:193], v131 offset:9216
	ds_read_b128 v[194:197], v131 offset:10240
	ds_read_b128 v[198:201], v131 offset:11264
	v_mfma_f32_32x32x16_bf16 v[32:47], v[202:205], v[80:83], v[32:47]
	v_cvt_pk_bf16_f32 v96, v0, v1
	v_cvt_pk_bf16_f32 v97, v2, v3
	v_cvt_pk_bf16_f32 v98, v4, v5
	v_cvt_pk_bf16_f32 v99, v6, v7
	v_cvt_pk_bf16_f32 v100, v8, v9
	v_mfma_f32_32x32x16_bf16 v[32:47], v[208:211], v[84:87], v[32:47]
	v_cvt_pk_bf16_f32 v101, v10, v11
	v_cvt_pk_bf16_f32 v102, v12, v13
	v_cvt_pk_bf16_f32 v103, v14, v15
	v_mfma_f32_32x32x16_bf16 v[48:63], v[212:215], v[80:83], v[48:63]
	v_cvt_pk_bf16_f32 v104, v16, v17
	v_cvt_pk_bf16_f32 v105, v18, v19
	v_cvt_pk_bf16_f32 v106, v20, v21
	v_cvt_pk_bf16_f32 v107, v22, v23
	v_cvt_pk_bf16_f32 v108, v24, v25
	v_mfma_f32_32x32x16_bf16 v[48:63], v[216:219], v[84:87], v[48:63]
	v_cvt_pk_bf16_f32 v109, v26, v27
	v_cvt_pk_bf16_f32 v110, v28, v29
	v_cvt_pk_bf16_f32 v111, v30, v31
	s_waitcnt lgkmcnt(4)
	ds_read_b128 v[202:205], v131 offset:12288
	ds_read_b128 v[208:211], v131 offset:13312
	ds_read_b128 v[212:215], v131 offset:14336
	ds_read_b128 v[216:219], v131 offset:15360
	v_mfma_f32_32x32x16_bf16 v[64:79], v[148:151], v[96:99], v[64:79]
	v_cvt_pk_bf16_f32 v112, v32, v33
	v_cvt_pk_bf16_f32 v113, v34, v35
	v_cvt_pk_bf16_f32 v114, v36, v37
	v_cvt_pk_bf16_f32 v115, v38, v39
	v_lshlrev_b32_e32 v80, 16, v88
	v_mfma_f32_32x32x16_bf16 v[64:79], v[152:155], v[100:103], v[64:79]
	v_cvt_pk_bf16_f32 v116, v40, v41
	v_cvt_pk_bf16_f32 v117, v42, v43
	v_cvt_pk_bf16_f32 v118, v44, v45
	v_cvt_pk_bf16_f32 v119, v46, v47
	v_and_b32_e32 v81, 0xffff0000, v88
	v_mfma_f32_32x32x16_bf16 v[64:79], v[156:159], v[104:107], v[64:79]
	v_cvt_pk_bf16_f32 v120, v48, v49
	v_cvt_pk_bf16_f32 v121, v50, v51
	v_cvt_pk_bf16_f32 v122, v52, v53
	v_cvt_pk_bf16_f32 v123, v54, v55
	v_lshlrev_b32_e32 v82, 16, v89
	v_mfma_f32_32x32x16_bf16 v[64:79], v[160:163], v[108:111], v[64:79]
	v_cvt_pk_bf16_f32 v124, v56, v57
	v_cvt_pk_bf16_f32 v125, v58, v59
	v_cvt_pk_bf16_f32 v126, v60, v61
	v_cvt_pk_bf16_f32 v127, v62, v63
	v_and_b32_e32 v83, 0xffff0000, v89
	ds_read_b128 v[148:151], v131 offset:16384
	ds_read_b128 v[152:155], v131 offset:17408
	ds_read_b128 v[156:159], v131 offset:20480
	ds_read_b128 v[160:163], v131 offset:21504
	v_mfma_f32_32x32x16_bf16 v[64:79], v[164:167], v[112:115], v[64:79]
	v_lshlrev_b32_e32 v84, 16, v90
	v_and_b32_e32 v85, 0xffff0000, v90
	v_lshlrev_b32_e32 v86, 16, v91
	v_and_b32_e32 v87, 0xffff0000, v91
	v_lshlrev_b32_e32 v88, 16, v92
	global_store_dwordx4 v128, v[96:99], s[8:9]
	v_mfma_f32_32x32x16_bf16 v[64:79], v[168:171], v[116:119], v[64:79]
	v_and_b32_e32 v89, 0xffff0000, v92
	v_lshlrev_b32_e32 v90, 16, v93
	v_and_b32_e32 v91, 0xffff0000, v93
	v_lshlrev_b32_e32 v92, 16, v94
	v_and_b32_e32 v93, 0xffff0000, v94
	global_store_dwordx4 v128, v[100:103], s[8:9] offset:1024
	v_mfma_f32_32x32x16_bf16 v[64:79], v[172:175], v[120:123], v[64:79]
	v_lshlrev_b32_e32 v94, 16, v95
	v_and_b32_e32 v95, 0xffff0000, v95
	global_store_dwordx4 v128, v[104:107], s[8:9] offset:2048
	global_store_dwordx4 v128, v[108:111], s[8:9] offset:3072
	v_mul_f32_e32 v0, v142, v0
	v_mfma_f32_32x32x16_bf16 v[64:79], v[178:181], v[124:127], v[64:79]
	v_mul_f32_e32 v1, v142, v1
	v_mul_f32_e32 v2, v142, v2
	v_mul_f32_e32 v3, v142, v3
	v_mul_f32_e32 v4, v142, v4
	v_mul_f32_e32 v5, v142, v5
	s_waitcnt lgkmcnt(8)
; DI bf16x8 packS(const f32x16& x, int s) { return pack8(x[8 * s], x[8 * s + 1], x[8 * s + 2], x[8 * s + 3], x[8 * s + 4], x[8 * s + 5], x[8 * s + 6], x[8 * s + 7]); }
; #define SCAN_MMK(F, mh) do { _Pragma("unroll") for (int q = 0; q < 4; ++q) { const int j2 = q >> 1, sx = q & 1; S[2 * (mh)] = MFMA32(F[q], Vb[j2][sx], S[2 * (mh)]); S[2 * (mh) + 1] = MFMA32(F[4 + q], Vb[j2][sx], S[2 * (mh) + 1]); } } while (0)
; DI void gdn_scan_seq(const Params& p, int bh16, char* ldsf) {
;     ...
;     bf16x8 Vb[2][2];
; #pragma unroll
;     for (int j2 = 0; j2 < 2; ++j2) { Vb[j2][0] = packS(vn[j2], 0); Vb[j2][1] = packS(vn[j2], 1); }
; #pragma unroll
;     for (int m = 0; m < 4; ++m)
; #pragma unroll
;       for (int r = 0; r < 16; ++r) S[m][r] *= gl;
;     SCAN_MMK(fa, 0);
;     SCAN_MMK(fb, 1);
;     ...
;     asm volatile("s_waitcnt lgkmcnt(0)" ::: "memory");
;     sl = sl == 2 ? 0 : sl + 1;
;   }
	ds_read_b128 v[164:167], v131 offset:24576
	ds_read_b128 v[168:171], v131 offset:25600
	ds_read_b128 v[172:175], v131 offset:28672
	ds_read_b128 v[178:181], v131 offset:29696
	v_mfma_f32_32x32x16_bf16 v[80:95], v[182:185], v[96:99], v[80:95]
	v_mul_f32_e32 v6, v142, v6
	v_mul_f32_e32 v7, v142, v7
	v_mul_f32_e32 v8, v142, v8
	v_mul_f32_e32 v9, v142, v9
	v_mul_f32_e32 v10, v142, v10
	v_mfma_f32_32x32x16_bf16 v[80:95], v[190:193], v[100:103], v[80:95]
	v_mul_f32_e32 v11, v142, v11
	v_mul_f32_e32 v12, v142, v12
	v_mul_f32_e32 v13, v142, v13
	v_mul_f32_e32 v14, v142, v14
	v_mul_f32_e32 v15, v142, v15
	v_mfma_f32_32x32x16_bf16 v[80:95], v[194:197], v[104:107], v[80:95]
	v_mul_f32_e32 v16, v142, v16
	v_mul_f32_e32 v17, v142, v17
	v_mul_f32_e32 v18, v142, v18
	v_mul_f32_e32 v19, v142, v19
	global_store_dwordx4 v128, v[112:115], s[10:11]
	v_mul_f32_e32 v32, v142, v32
	v_mfma_f32_32x32x16_bf16 v[80:95], v[198:201], v[108:111], v[80:95]
	v_mul_f32_e32 v20, v142, v20
	v_mul_f32_e32 v21, v142, v21
	v_mul_f32_e32 v22, v142, v22
	v_mul_f32_e32 v23, v142, v23
	global_store_dwordx4 v128, v[116:119], s[10:11] offset:1024
	v_mul_f32_e32 v33, v142, v33
	s_waitcnt lgkmcnt(8)
	ds_read_b128 v[182:185], v131 offset:18432
	ds_read_b128 v[190:193], v131 offset:19456
	ds_read_b128 v[194:197], v131 offset:22528
	ds_read_b128 v[198:201], v131 offset:23552
	v_mfma_f32_32x32x16_bf16 v[80:95], v[202:205], v[112:115], v[80:95]
	v_mul_f32_e32 v24, v142, v24
	v_mul_f32_e32 v25, v142, v25
	v_mul_f32_e32 v26, v142, v26
	v_mul_f32_e32 v27, v142, v27
	global_store_dwordx4 v128, v[120:123], s[10:11] offset:2048
	v_mul_f32_e32 v34, v142, v34
	v_mfma_f32_32x32x16_bf16 v[80:95], v[208:211], v[116:119], v[80:95]
	v_mul_f32_e32 v28, v142, v28
	v_mul_f32_e32 v29, v142, v29
	v_mul_f32_e32 v30, v142, v30
	v_mul_f32_e32 v31, v142, v31
	global_store_dwordx4 v128, v[124:127], s[10:11] offset:3072
	v_mul_f32_e32 v35, v142, v35
	v_mfma_f32_32x32x16_bf16 v[80:95], v[212:215], v[120:123], v[80:95]
	v_cvt_pk_bf16_f32 v64, v64, v65
	v_cvt_pk_bf16_f32 v65, v66, v67
	v_cvt_pk_bf16_f32 v66, v68, v69
	v_cvt_pk_bf16_f32 v67, v70, v71
	v_cvt_pk_bf16_f32 v68, v72, v73
	v_mul_f32_e32 v36, v142, v36
	v_mfma_f32_32x32x16_bf16 v[80:95], v[216:219], v[124:127], v[80:95]
	v_cvt_pk_bf16_f32 v69, v74, v75
	v_cvt_pk_bf16_f32 v70, v76, v77
	v_cvt_pk_bf16_f32 v71, v78, v79
	v_mul_f32_e32 v37, v142, v37
	v_mul_f32_e32 v38, v142, v38
	v_mul_f32_e32 v39, v142, v39
	s_waitcnt lgkmcnt(8)
	ds_read_b128 v[202:205], v131 offset:26624
	ds_read_b128 v[208:211], v131 offset:27648
	ds_read_b128 v[212:215], v131 offset:30720
	ds_read_b128 v[216:219], v131 offset:31744
	v_mfma_f32_32x32x16_bf16 v[0:15], v[148:151], v[64:67], v[0:15]
	v_mul_f32_e32 v40, v142, v40
	v_mul_f32_e32 v41, v142, v41
	v_mul_f32_e32 v42, v142, v42
	v_mul_f32_e32 v43, v142, v43
	v_mul_f32_e32 v44, v142, v44
	v_mul_f32_e32 v45, v142, v45
	s_add_u32 s2, s2, 1
	s_xor_b32 s3, s3, 0xc000
	s_add_u32 s18, s18, 4
	s_add_u32 s8, s8, 0x8000
	s_addc_u32 s9, s9, 0
	s_add_u32 s10, s10, 0x8000
	s_addc_u32 s11, s11, 0
	v_mfma_f32_32x32x16_bf16 v[0:15], v[152:155], v[68:71], v[0:15]
	v_mul_f32_e32 v46, v142, v46
	v_mul_f32_e32 v47, v142, v47
	v_mul_f32_e32 v48, v142, v48
	v_mul_f32_e32 v49, v142, v49
	v_mul_f32_e32 v50, v142, v50
	v_mul_f32_e32 v51, v142, v51
	v_mfma_f32_32x32x16_bf16 v[16:31], v[156:159], v[64:67], v[16:31]
	v_mul_f32_e32 v52, v142, v52
	v_mul_f32_e32 v53, v142, v53
	v_mul_f32_e32 v54, v142, v54
	v_mul_f32_e32 v55, v142, v55
	v_mul_f32_e32 v56, v142, v56
	v_mul_f32_e32 v57, v142, v57
	v_mfma_f32_32x32x16_bf16 v[16:31], v[160:163], v[68:71], v[16:31]
	v_mul_f32_e32 v58, v142, v58
	v_mul_f32_e32 v59, v142, v59
	v_mul_f32_e32 v60, v142, v60
	v_mul_f32_e32 v61, v142, v61
	v_mul_f32_e32 v62, v142, v62
	v_mul_f32_e32 v63, v142, v63
	s_waitcnt lgkmcnt(8)
	v_mfma_f32_32x32x16_bf16 v[32:47], v[164:167], v[64:67], v[32:47]
	v_cvt_pk_bf16_f32 v80, v80, v81
	v_cvt_pk_bf16_f32 v81, v82, v83
	v_cvt_pk_bf16_f32 v82, v84, v85
	v_cvt_pk_bf16_f32 v83, v86, v87
	v_cvt_pk_bf16_f32 v84, v88, v89
	v_cvt_pk_bf16_f32 v85, v90, v91
	v_mfma_f32_32x32x16_bf16 v[32:47], v[168:171], v[68:71], v[32:47]
	v_cvt_pk_bf16_f32 v86, v92, v93
	v_cvt_pk_bf16_f32 v87, v94, v95
	v_mfma_f32_32x32x16_bf16 v[48:63], v[172:175], v[64:67], v[48:63]
	v_mfma_f32_32x32x16_bf16 v[48:63], v[178:181], v[68:71], v[48:63]
	s_cmp_lt_u32 s2, 0x80
	s_waitcnt lgkmcnt(0)
	s_cbranch_scc1 .Lscan_loop
	s_setprio 0
	s_branch .Lscan_end
